# topk rank counting: first compare of each pair to a free SGPR pair, hazard nops removed (425 -> 48 s_nop 1)
# baseline (speedup 1.0000x reference)
.LBB0_1854:
	v_cndmask_b32_e64 v153, 0, v153, s[0:1]
	v_cndmask_b32_e64 v154, 0, v154, s[0:1]
	v_cndmask_b32_e64 v153, v153, v157, s[54:55]
	v_cndmask_b32_e64 v155, 0, v155, s[0:1]
	v_cndmask_b32_e64 v154, v154, v158, s[54:55]
	v_cndmask_b32_e64 v153, v153, v161, s[64:65]
	v_cndmask_b32_e64 v155, v155, v159, s[54:55]
	v_cndmask_b32_e64 v154, v154, v162, s[64:65]
	v_cndmask_b32_e64 v153, v153, v165, s[2:3]
	v_cndmask_b32_e64 v155, v155, v163, s[64:65]
	v_cndmask_b32_e64 v154, v154, v166, s[2:3]
	v_cndmask_b32_e64 v153, v153, v169, s[6:7]
	v_cndmask_b32_e64 v155, v155, v167, s[2:3]
	v_cndmask_b32_e64 v154, v154, v170, s[6:7]
	v_cndmask_b32_e64 v153, v153, v173, s[96:97]
	v_cndmask_b32_e64 v156, 0, v156, s[0:1]
	v_cndmask_b32_e64 v155, v155, v171, s[6:7]
	v_cndmask_b32_e64 v154, v154, v174, s[96:97]
	v_cndmask_b32_e64 v153, v153, v177, s[66:67]
	v_cndmask_b32_e64 v156, v156, v160, s[54:55]
	v_cndmask_b32_e64 v155, v155, v175, s[96:97]
	v_cndmask_b32_e64 v154, v154, v178, s[66:67]
	v_cndmask_b32_e64 v153, v153, v181, s[24:25]
	v_cndmask_b32_e64 v156, v156, v164, s[64:65]
	v_cndmask_b32_e64 v155, v155, v179, s[66:67]
	v_cndmask_b32_e64 v154, v154, v182, s[24:25]
	v_cndmask_b32_e64 v153, v153, v185, s[26:27]
	v_cndmask_b32_e64 v156, v156, v168, s[2:3]
	v_cndmask_b32_e64 v155, v155, v183, s[24:25]
	v_cndmask_b32_e64 v154, v154, v186, s[26:27]
	v_cndmask_b32_e64 v153, v153, v189, s[28:29]
	v_cndmask_b32_e64 v156, v156, v172, s[6:7]
	v_cndmask_b32_e64 v155, v155, v187, s[26:27]
	v_cndmask_b32_e64 v154, v154, v190, s[28:29]
	v_cndmask_b32_e64 v153, v153, v193, s[30:31]
	v_cndmask_b32_e64 v156, v156, v176, s[96:97]
	v_cndmask_b32_e64 v155, v155, v191, s[28:29]
	v_cndmask_b32_e64 v154, v154, v194, s[30:31]
	v_cndmask_b32_e64 v153, v153, v197, s[34:35]
	v_cndmask_b32_e64 v156, v156, v180, s[66:67]
	v_cndmask_b32_e64 v155, v155, v195, s[30:31]
	v_cndmask_b32_e64 v154, v154, v198, s[34:35]
	v_cndmask_b32_e64 v153, v153, v206, s[36:37]
	v_cndmask_b32_e64 v156, v156, v184, s[24:25]
	v_cndmask_b32_e64 v155, v155, v199, s[34:35]
	v_cndmask_b32_e64 v154, v154, v207, s[36:37]
	v_cndmask_b32_e64 v153, v153, v210, s[38:39]
	v_cndmask_b32_e64 v156, v156, v188, s[26:27]
	v_cndmask_b32_e64 v155, v155, v208, s[36:37]
	v_cndmask_b32_e64 v154, v154, v211, s[38:39]
	v_cndmask_b32_e64 v153, v153, v214, s[40:41]
	v_max_i32_e32 v157, v218, v219
	v_cndmask_b32_e64 v156, v156, v192, s[28:29]
	v_cndmask_b32_e64 v155, v155, v212, s[38:39]
	v_cndmask_b32_e64 v154, v154, v215, s[40:41]
	v_cndmask_b32_e64 v153, v153, v157, s[42:43]
	v_max_i32_e32 v157, v220, v221
	v_cndmask_b32_e64 v156, v156, v196, s[30:31]
	v_cndmask_b32_e64 v155, v155, v216, s[40:41]
	v_cndmask_b32_e64 v157, v154, v157, s[42:43]
	v_max_i32_e32 v154, v240, v241
	ds_bpermute_b32 v158, v146, v153
	v_cndmask_b32_e64 v156, v156, v203, s[34:35]
	v_cndmask_b32_e64 v159, v155, v154, s[42:43]
	ds_bpermute_b32 v154, v147, v153
	v_cndmask_b32_e64 v156, v156, v209, s[36:37]
	v_cndmask_b32_e64 v156, v156, v213, s[38:39]
	v_cndmask_b32_e64 v156, v156, v217, s[40:41]
	v_max_i32_e32 v155, v222, v223
	v_cndmask_b32_e64 v167, v156, v155, s[42:43]
	s_waitcnt lgkmcnt(1)
	v_lshlrev_b32_e32 v155, 7, v158
	v_and_b32_e32 v155, 0x3f80, v155
	s_waitcnt lgkmcnt(0)
	v_and_b32_e32 v156, 0x7f, v154
	s_movk_i32 s9, 0x3fff
	v_bitop3_b32 v184, v156, s9, v155 bitop3:0x36
	v_ashrrev_i32_e32 v155, 31, v154
	v_ashrrev_i32_e32 v156, 31, v158
	v_and_b32_e32 v155, 0x7fffffff, v155
	v_and_b32_e32 v156, 0x7fffffff, v156
	v_xor_b32_e32 v155, v155, v154
	v_xor_b32_e32 v154, v156, v158
	ds_bpermute_b32 v156, v148, v153
	ds_bpermute_b32 v153, v149, v153
	v_pk_add_f32 v[154:155], v[154:155], v[154:155] op_sel:[1,0] op_sel_hi:[0,1]
	s_movk_i32 s10, 0xffc0
	v_and_or_b32 v154, v154, s10, v141
	v_cndmask_b32_e64 v185, v238, v154, s[4:5]
	s_waitcnt lgkmcnt(1)
	v_lshlrev_b32_e32 v154, 7, v156
	v_and_b32_e32 v154, 0x3f80, v154
	s_waitcnt lgkmcnt(0)
	v_and_b32_e32 v155, 0x7f, v153
	v_bitop3_b32 v166, v155, s9, v154 bitop3:0x36
	v_ashrrev_i32_e32 v154, 31, v153
	v_ashrrev_i32_e32 v155, 31, v156
	v_and_b32_e32 v154, 0x7fffffff, v154
	v_and_b32_e32 v158, 0x7fffffff, v155
	v_xor_b32_e32 v155, v154, v153
	v_xor_b32_e32 v154, v158, v156
	v_pk_add_f32 v[154:155], v[154:155], v[154:155] op_sel:[1,0] op_sel_hi:[0,1]
	ds_bpermute_b32 v153, v146, v157
	ds_bpermute_b32 v155, v147, v157
	v_and_or_b32 v154, v154, s10, v141
	v_cndmask_b32_e64 v186, v238, v154, s[4:5]
	ds_bpermute_b32 v187, v149, v167
	s_waitcnt lgkmcnt(2)
	v_lshlrev_b32_e32 v154, 7, v153
	v_and_b32_e32 v154, 0x3f80, v154
	s_waitcnt lgkmcnt(1)
	v_and_b32_e32 v156, 0x7f, v155
	v_bitop3_b32 v164, v156, s9, v154 bitop3:0x36
	v_ashrrev_i32_e32 v154, 31, v155
	v_ashrrev_i32_e32 v156, 31, v153
	v_and_b32_e32 v154, 0x7fffffff, v154
	v_and_b32_e32 v156, 0x7fffffff, v156
	v_xor_b32_e32 v155, v154, v155
	v_xor_b32_e32 v154, v156, v153
	ds_bpermute_b32 v153, v148, v157
	v_pk_add_f32 v[154:155], v[154:155], v[154:155] op_sel:[1,0] op_sel_hi:[0,1]
	ds_bpermute_b32 v155, v149, v157
	v_and_or_b32 v154, v154, s10, v141
	v_cndmask_b32_e64 v165, v238, v154, s[4:5]
	s_waitcnt lgkmcnt(1)
	v_lshlrev_b32_e32 v154, 7, v153
	v_and_b32_e32 v154, 0x3f80, v154
	s_waitcnt lgkmcnt(0)
	v_and_b32_e32 v156, 0x7f, v155
	v_bitop3_b32 v162, v156, s9, v154 bitop3:0x36
	v_ashrrev_i32_e32 v154, 31, v155
	v_ashrrev_i32_e32 v156, 31, v153
	v_and_b32_e32 v154, 0x7fffffff, v154
	v_and_b32_e32 v156, 0x7fffffff, v156
	v_xor_b32_e32 v155, v154, v155
	v_xor_b32_e32 v154, v156, v153
	v_pk_add_f32 v[154:155], v[154:155], v[154:155] op_sel:[1,0] op_sel_hi:[0,1]
	ds_bpermute_b32 v153, v146, v159
	ds_bpermute_b32 v155, v147, v159
	v_and_or_b32 v154, v154, s10, v141
	v_cndmask_b32_e64 v163, v238, v154, s[4:5]
	ds_write2st64_b32 v142, v185, v186 offset1:1
	s_waitcnt lgkmcnt(2)
	v_lshlrev_b32_e32 v154, 7, v153
	v_and_b32_e32 v154, 0x3f80, v154
	s_waitcnt lgkmcnt(1)
	v_and_b32_e32 v156, 0x7f, v155
	v_bitop3_b32 v160, v156, s9, v154 bitop3:0x36
	v_ashrrev_i32_e32 v154, 31, v155
	v_ashrrev_i32_e32 v156, 31, v153
	v_and_b32_e32 v154, 0x7fffffff, v154
	v_and_b32_e32 v156, 0x7fffffff, v156
	v_xor_b32_e32 v155, v154, v155
	v_xor_b32_e32 v154, v156, v153
	ds_bpermute_b32 v153, v148, v159
	v_pk_add_f32 v[154:155], v[154:155], v[154:155] op_sel:[1,0] op_sel_hi:[0,1]
	ds_bpermute_b32 v155, v149, v159
	v_and_or_b32 v154, v154, s10, v141
	v_cndmask_b32_e64 v161, v238, v154, s[4:5]
	s_waitcnt lgkmcnt(1)
	v_lshlrev_b32_e32 v154, 7, v153
	v_and_b32_e32 v154, 0x3f80, v154
	s_waitcnt lgkmcnt(0)
	v_and_b32_e32 v156, 0x7f, v155
	v_bitop3_b32 v158, v156, s9, v154 bitop3:0x36
	v_ashrrev_i32_e32 v154, 31, v155
	v_ashrrev_i32_e32 v156, 31, v153
	v_and_b32_e32 v154, 0x7fffffff, v154
	v_and_b32_e32 v156, 0x7fffffff, v156
	v_xor_b32_e32 v155, v154, v155
	v_xor_b32_e32 v154, v156, v153
	ds_bpermute_b32 v153, v146, v167
	ds_bpermute_b32 v156, v147, v167
	v_pk_add_f32 v[154:155], v[154:155], v[154:155] op_sel:[1,0] op_sel_hi:[0,1]
	v_and_or_b32 v154, v154, s10, v141
	v_cndmask_b32_e64 v159, v238, v154, s[4:5]
	s_waitcnt lgkmcnt(1)
	v_lshlrev_b32_e32 v154, 7, v153
	v_and_b32_e32 v154, 0x3f80, v154
	s_waitcnt lgkmcnt(0)
	v_and_b32_e32 v155, 0x7f, v156
	v_bitop3_b32 v155, v155, s9, v154 bitop3:0x36
	v_ashrrev_i32_e32 v154, 31, v156
	v_ashrrev_i32_e32 v157, 31, v153
	ds_bpermute_b32 v167, v148, v167
	v_and_b32_e32 v154, 0x7fffffff, v154
	v_and_b32_e32 v168, 0x7fffffff, v157
	v_xor_b32_e32 v157, v154, v156
	v_xor_b32_e32 v156, v168, v153
	v_pk_add_f32 v[156:157], v[156:157], v[156:157] op_sel:[1,0] op_sel_hi:[0,1]
	v_and_or_b32 v153, v156, s10, v141
	v_cndmask_b32_e64 v157, v238, v153, s[4:5]
	v_ashrrev_i32_e32 v153, 31, v187
	s_waitcnt lgkmcnt(0)
	v_ashrrev_i32_e32 v154, 31, v167
	v_and_b32_e32 v153, 0x7fffffff, v153
	v_and_b32_e32 v154, 0x7fffffff, v154
	v_xor_b32_e32 v169, v153, v187
	v_xor_b32_e32 v168, v154, v167
	v_pk_add_f32 v[168:169], v[168:169], v[168:169] op_sel:[1,0] op_sel_hi:[0,1]
	v_and_or_b32 v153, v168, s10, v141
	v_cndmask_b32_e64 v153, v238, v153, s[4:5]
	ds_write2st64_b32 v142, v165, v163 offset0:2 offset1:3
	ds_write2st64_b32 v142, v161, v159 offset0:4 offset1:5
	ds_write2st64_b32 v142, v157, v153 offset0:6 offset1:7
	s_waitcnt lgkmcnt(0)
	v_mov_b32_e32 v154, s84
	ds_read_b128 v[168:171], v154
	v_lshlrev_b32_e32 v156, 7, v167
	ds_read_b128 v[172:175], v154 offset:16
	ds_read_b128 v[176:179], v154 offset:32
	ds_read_b128 v[180:183], v154 offset:48
	v_and_b32_e32 v156, 0x3f80, v156
	s_waitcnt lgkmcnt(3)
	v_cmp_gt_f32_e64 s[16:17], v169, v185
	v_cmp_gt_f32_e32 vcc, v168, v185
	v_cmp_gt_f32_e64 s[98:99], v170, v185
	v_cndmask_b32_e64 v167, 0, 1, s[16:17]
	v_addc_co_u32_e32 v167, vcc, 0, v167, vcc
	v_cmp_gt_f32_e32 vcc, v171, v185
	v_cndmask_b32_e64 v168, 0, 1, s[98:99]
	s_nop 0
	v_addc_co_u32_e32 v167, vcc, v167, v168, vcc
	s_waitcnt lgkmcnt(2)
	v_cmp_gt_f32_e64 s[16:17], v172, v185
	v_cmp_gt_f32_e32 vcc, v173, v185
	v_cmp_gt_f32_e64 s[98:99], v174, v185
	v_cndmask_b32_e64 v168, 0, 1, s[16:17]
	v_addc_co_u32_e32 v167, vcc, v167, v168, vcc
	v_cmp_gt_f32_e32 vcc, v175, v185
	v_cndmask_b32_e64 v168, 0, 1, s[98:99]
	s_nop 0
	v_addc_co_u32_e32 v167, vcc, v167, v168, vcc
	s_waitcnt lgkmcnt(1)
	v_cmp_gt_f32_e64 s[16:17], v176, v185
	v_cmp_gt_f32_e32 vcc, v177, v185
	v_cmp_gt_f32_e64 s[98:99], v178, v185
	v_cndmask_b32_e64 v168, 0, 1, s[16:17]
	v_addc_co_u32_e32 v167, vcc, v167, v168, vcc
	v_cmp_gt_f32_e32 vcc, v179, v185
	v_cndmask_b32_e64 v168, 0, 1, s[98:99]
	s_nop 0
	v_addc_co_u32_e32 v167, vcc, v167, v168, vcc
	s_waitcnt lgkmcnt(0)
	v_cmp_gt_f32_e64 s[16:17], v180, v185
	v_cmp_gt_f32_e32 vcc, v181, v185
	s_nop 0
	v_cndmask_b32_e64 v168, 0, 1, s[16:17]
	v_addc_co_u32_e32 v167, vcc, v167, v168, vcc
	ds_read_b128 v[168:171], v154 offset:64
	v_cmp_gt_f32_e64 s[16:17], v182, v185
	v_cmp_gt_f32_e32 vcc, v183, v185
	s_nop 0
	v_cndmask_b32_e64 v172, 0, 1, s[16:17]
	v_addc_co_u32_e32 v167, vcc, v167, v172, vcc
	ds_read_b128 v[172:175], v154 offset:80
	s_waitcnt lgkmcnt(1)
	v_cmp_gt_f32_e64 s[16:17], v168, v185
	v_cmp_gt_f32_e32 vcc, v169, v185
	v_cmp_gt_f32_e64 s[98:99], v170, v185
	v_cndmask_b32_e64 v168, 0, 1, s[16:17]
	v_addc_co_u32_e32 v167, vcc, v167, v168, vcc
	v_cmp_gt_f32_e32 vcc, v171, v185
	v_cndmask_b32_e64 v168, 0, 1, s[98:99]
	s_nop 0
	v_addc_co_u32_e32 v167, vcc, v167, v168, vcc
	s_waitcnt lgkmcnt(0)
	v_cmp_gt_f32_e64 s[16:17], v172, v185
	v_cmp_gt_f32_e32 vcc, v173, v185
	s_nop 0
	v_cndmask_b32_e64 v168, 0, 1, s[16:17]
	v_addc_co_u32_e32 v167, vcc, v167, v168, vcc
	ds_read_b128 v[168:171], v154 offset:96
	v_cmp_gt_f32_e64 s[16:17], v174, v185
	v_cmp_gt_f32_e32 vcc, v175, v185
	s_nop 0
	v_cndmask_b32_e64 v172, 0, 1, s[16:17]
	v_addc_co_u32_e32 v167, vcc, v167, v172, vcc
	ds_read_b128 v[172:175], v154 offset:112
	s_waitcnt lgkmcnt(1)
	v_cmp_gt_f32_e64 s[16:17], v168, v185
	v_cmp_gt_f32_e32 vcc, v169, v185
	v_cmp_gt_f32_e64 s[98:99], v170, v185
	v_cndmask_b32_e64 v168, 0, 1, s[16:17]
	v_addc_co_u32_e32 v167, vcc, v167, v168, vcc
	v_cmp_gt_f32_e32 vcc, v171, v185
	v_cndmask_b32_e64 v168, 0, 1, s[98:99]
	s_nop 0
	v_addc_co_u32_e32 v167, vcc, v167, v168, vcc
	s_waitcnt lgkmcnt(0)
	v_cmp_gt_f32_e64 s[16:17], v172, v185
	v_cmp_gt_f32_e32 vcc, v173, v185
	s_nop 0
	v_cndmask_b32_e64 v168, 0, 1, s[16:17]
	v_addc_co_u32_e32 v167, vcc, v167, v168, vcc
	ds_read_b128 v[168:171], v154 offset:128
	v_cmp_gt_f32_e64 s[16:17], v174, v185
	v_cmp_gt_f32_e32 vcc, v175, v185
	s_nop 0
	v_cndmask_b32_e64 v172, 0, 1, s[16:17]
	v_addc_co_u32_e32 v167, vcc, v167, v172, vcc
	ds_read_b128 v[172:175], v154 offset:144
	s_waitcnt lgkmcnt(1)
	v_cmp_gt_f32_e64 s[16:17], v168, v185
	v_cmp_gt_f32_e32 vcc, v169, v185
	v_cmp_gt_f32_e64 s[98:99], v170, v185
	v_cndmask_b32_e64 v168, 0, 1, s[16:17]
	v_addc_co_u32_e32 v167, vcc, v167, v168, vcc
	v_cmp_gt_f32_e32 vcc, v171, v185
	v_cndmask_b32_e64 v168, 0, 1, s[98:99]
	s_nop 0
	v_addc_co_u32_e32 v167, vcc, v167, v168, vcc
	s_waitcnt lgkmcnt(0)
	v_cmp_gt_f32_e64 s[16:17], v172, v185
	v_cmp_gt_f32_e32 vcc, v173, v185
	s_nop 0
	v_cndmask_b32_e64 v168, 0, 1, s[16:17]
	v_addc_co_u32_e32 v167, vcc, v167, v168, vcc
	ds_read_b128 v[168:171], v154 offset:160
	v_cmp_gt_f32_e64 s[16:17], v174, v185
	v_cmp_gt_f32_e32 vcc, v175, v185
	s_nop 0
	v_cndmask_b32_e64 v172, 0, 1, s[16:17]
	v_addc_co_u32_e32 v167, vcc, v167, v172, vcc
	ds_read_b128 v[172:175], v154 offset:176
	s_waitcnt lgkmcnt(1)
	v_cmp_gt_f32_e64 s[16:17], v168, v185
	v_cmp_gt_f32_e32 vcc, v169, v185
	v_cmp_gt_f32_e64 s[98:99], v170, v185
	v_cndmask_b32_e64 v168, 0, 1, s[16:17]
	v_addc_co_u32_e32 v167, vcc, v167, v168, vcc
	v_cmp_gt_f32_e32 vcc, v171, v185
	v_cndmask_b32_e64 v168, 0, 1, s[98:99]
	s_nop 0
	v_addc_co_u32_e32 v167, vcc, v167, v168, vcc
	s_waitcnt lgkmcnt(0)
	v_cmp_gt_f32_e64 s[16:17], v172, v185
	v_cmp_gt_f32_e32 vcc, v173, v185
	s_nop 0
	v_cndmask_b32_e64 v168, 0, 1, s[16:17]
	v_addc_co_u32_e32 v167, vcc, v167, v168, vcc
	ds_read_b128 v[168:171], v154 offset:192
	v_cmp_gt_f32_e64 s[16:17], v174, v185
	v_cmp_gt_f32_e32 vcc, v175, v185
	s_nop 0
	v_cndmask_b32_e64 v172, 0, 1, s[16:17]
	v_addc_co_u32_e32 v167, vcc, v167, v172, vcc
	ds_read_b128 v[172:175], v154 offset:256
	s_waitcnt lgkmcnt(1)
	v_cmp_gt_f32_e32 vcc, v168, v185
	s_nop 1
	v_cndmask_b32_e64 v168, 0, 1, vcc
	v_cmp_gt_f32_e32 vcc, v169, v185
	v_and_b32_e32 v169, 0x7f, v187
	v_bitop3_b32 v156, v169, s9, v156 bitop3:0x36
	v_addc_co_u32_e32 v167, vcc, v167, v168, vcc
	v_cmp_gt_f32_e64 s[16:17], v170, v185
	v_cmp_gt_f32_e32 vcc, v171, v185
	s_nop 0
	v_cndmask_b32_e64 v168, 0, 1, s[16:17]
	v_addc_co_u32_e32 v167, vcc, v167, v168, vcc
	v_cmp_gt_u32_e32 vcc, 16, v167
	s_and_b64 vcc, s[4:5], vcc
	s_nop 0
	v_cndmask_b32_e32 v167, v150, v167, vcc
	v_lshlrev_b32_e32 v167, 2, v167
	ds_permute_b32 v168, v167, v185
	s_waitcnt lgkmcnt(1)
	v_cmp_gt_f32_e32 vcc, v173, v186
	ds_permute_b32 v176, v167, v184
	s_waitcnt lgkmcnt(1)
	v_cndmask_b32_e64 v177, 0, v168, s[44:45]
	v_cndmask_b32_e64 v167, 0, 1, vcc
	v_cmp_gt_f32_e32 vcc, v172, v186
	ds_read_b128 v[168:171], v154 offset:272
	s_nop 0
	v_addc_co_u32_e32 v167, vcc, 0, v167, vcc
	v_cmp_gt_f32_e64 s[16:17], v174, v186
	v_cmp_gt_f32_e32 vcc, v175, v186
	s_nop 0
	v_cndmask_b32_e64 v172, 0, 1, s[16:17]
	v_addc_co_u32_e32 v167, vcc, v167, v172, vcc
	ds_read_b128 v[172:175], v154 offset:288
	s_waitcnt lgkmcnt(1)
	v_cmp_gt_f32_e64 s[16:17], v168, v186
	v_cmp_gt_f32_e32 vcc, v169, v186
	v_cmp_gt_f32_e64 s[98:99], v170, v186
	v_cndmask_b32_e64 v168, 0, 1, s[16:17]
	v_addc_co_u32_e32 v167, vcc, v167, v168, vcc
	v_cmp_gt_f32_e32 vcc, v171, v186
	v_cndmask_b32_e64 v168, 0, 1, s[98:99]
	s_nop 0
	v_addc_co_u32_e32 v167, vcc, v167, v168, vcc
	s_waitcnt lgkmcnt(0)
	v_cmp_gt_f32_e64 s[16:17], v172, v186
	v_cmp_gt_f32_e32 vcc, v173, v186
	s_nop 0
	v_cndmask_b32_e64 v168, 0, 1, s[16:17]
	v_addc_co_u32_e32 v167, vcc, v167, v168, vcc
	ds_read_b128 v[168:171], v154 offset:304
	v_cmp_gt_f32_e64 s[16:17], v174, v186
	v_cmp_gt_f32_e32 vcc, v175, v186
	s_nop 0
	v_cndmask_b32_e64 v172, 0, 1, s[16:17]
	v_addc_co_u32_e32 v167, vcc, v167, v172, vcc
	ds_read_b128 v[172:175], v154 offset:320
	s_waitcnt lgkmcnt(1)
	v_cmp_gt_f32_e64 s[16:17], v168, v186
	v_cmp_gt_f32_e32 vcc, v169, v186
	v_cmp_gt_f32_e64 s[98:99], v170, v186
	v_cndmask_b32_e64 v168, 0, 1, s[16:17]
	v_addc_co_u32_e32 v167, vcc, v167, v168, vcc
	v_cmp_gt_f32_e32 vcc, v171, v186
	v_cndmask_b32_e64 v168, 0, 1, s[98:99]
	s_nop 0
	v_addc_co_u32_e32 v167, vcc, v167, v168, vcc
	s_waitcnt lgkmcnt(0)
	v_cmp_gt_f32_e64 s[16:17], v172, v186
	v_cmp_gt_f32_e32 vcc, v173, v186
	s_nop 0
	v_cndmask_b32_e64 v168, 0, 1, s[16:17]
	v_addc_co_u32_e32 v167, vcc, v167, v168, vcc
	ds_read_b128 v[168:171], v154 offset:336
	v_cmp_gt_f32_e64 s[16:17], v174, v186
	v_cmp_gt_f32_e32 vcc, v175, v186
	s_nop 0
	v_cndmask_b32_e64 v172, 0, 1, s[16:17]
	v_addc_co_u32_e32 v167, vcc, v167, v172, vcc
	ds_read_b128 v[172:175], v154 offset:352
	s_waitcnt lgkmcnt(1)
	v_cmp_gt_f32_e64 s[16:17], v168, v186
	v_cmp_gt_f32_e32 vcc, v169, v186
	v_cmp_gt_f32_e64 s[98:99], v170, v186
	v_cndmask_b32_e64 v168, 0, 1, s[16:17]
	v_addc_co_u32_e32 v167, vcc, v167, v168, vcc
	v_cmp_gt_f32_e32 vcc, v171, v186
	v_cndmask_b32_e64 v168, 0, 1, s[98:99]
	s_nop 0
	v_addc_co_u32_e32 v167, vcc, v167, v168, vcc
	s_waitcnt lgkmcnt(0)
	v_cmp_gt_f32_e64 s[16:17], v172, v186
	v_cmp_gt_f32_e32 vcc, v173, v186
	s_nop 0
	v_cndmask_b32_e64 v168, 0, 1, s[16:17]
	v_addc_co_u32_e32 v167, vcc, v167, v168, vcc
	ds_read_b128 v[168:171], v154 offset:368
	v_cmp_gt_f32_e64 s[16:17], v174, v186
	v_cmp_gt_f32_e32 vcc, v175, v186
	s_nop 0
	v_cndmask_b32_e64 v172, 0, 1, s[16:17]
	v_addc_co_u32_e32 v167, vcc, v167, v172, vcc
	ds_read_b128 v[172:175], v154 offset:384
	s_waitcnt lgkmcnt(1)
	v_cmp_gt_f32_e64 s[16:17], v168, v186
	v_cmp_gt_f32_e32 vcc, v169, v186
	v_cmp_gt_f32_e64 s[98:99], v170, v186
	v_cndmask_b32_e64 v168, 0, 1, s[16:17]
	v_addc_co_u32_e32 v167, vcc, v167, v168, vcc
	v_cmp_gt_f32_e32 vcc, v171, v186
	v_cndmask_b32_e64 v168, 0, 1, s[98:99]
	s_nop 0
	v_addc_co_u32_e32 v167, vcc, v167, v168, vcc
	s_waitcnt lgkmcnt(0)
	v_cmp_gt_f32_e64 s[16:17], v172, v186
	v_cmp_gt_f32_e32 vcc, v173, v186
	s_nop 0
	v_cndmask_b32_e64 v168, 0, 1, s[16:17]
	v_addc_co_u32_e32 v167, vcc, v167, v168, vcc
	ds_read_b128 v[168:171], v154 offset:400
	v_cmp_gt_f32_e64 s[16:17], v174, v186
	v_cmp_gt_f32_e32 vcc, v175, v186
	s_nop 0
	v_cndmask_b32_e64 v172, 0, 1, s[16:17]
	v_addc_co_u32_e32 v167, vcc, v167, v172, vcc
	ds_read_b128 v[172:175], v154 offset:416
	s_waitcnt lgkmcnt(1)
	v_cmp_gt_f32_e64 s[16:17], v168, v186
	v_cmp_gt_f32_e32 vcc, v169, v186
	v_cmp_gt_f32_e64 s[98:99], v170, v186
	v_cndmask_b32_e64 v168, 0, 1, s[16:17]
	v_addc_co_u32_e32 v167, vcc, v167, v168, vcc
	v_cmp_gt_f32_e32 vcc, v171, v186
	v_cndmask_b32_e64 v168, 0, 1, s[98:99]
	s_nop 0
	v_addc_co_u32_e32 v167, vcc, v167, v168, vcc
	s_waitcnt lgkmcnt(0)
	v_cmp_gt_f32_e64 s[16:17], v172, v186
	v_cmp_gt_f32_e32 vcc, v173, v186
	s_nop 0
	v_cndmask_b32_e64 v168, 0, 1, s[16:17]
	v_addc_co_u32_e32 v167, vcc, v167, v168, vcc
	ds_read_b128 v[168:171], v154 offset:432
	v_cmp_gt_f32_e64 s[16:17], v174, v186
	v_cmp_gt_f32_e32 vcc, v175, v186
	s_nop 0
	v_cndmask_b32_e64 v172, 0, 1, s[16:17]
	v_addc_co_u32_e32 v167, vcc, v167, v172, vcc
	ds_read_b128 v[172:175], v154 offset:448
	s_waitcnt lgkmcnt(1)
	v_cmp_gt_f32_e64 s[16:17], v168, v186
	v_cmp_gt_f32_e32 vcc, v169, v186
	v_cmp_gt_f32_e64 s[98:99], v170, v186
	v_cndmask_b32_e64 v168, 0, 1, s[16:17]
	v_addc_co_u32_e32 v167, vcc, v167, v168, vcc
	v_cmp_gt_f32_e32 vcc, v171, v186
	v_cndmask_b32_e64 v168, 0, 1, s[98:99]
	s_nop 0
	v_addc_co_u32_e32 v167, vcc, v167, v168, vcc
	s_waitcnt lgkmcnt(0)
	v_cmp_gt_f32_e64 s[16:17], v172, v186
	v_cmp_gt_f32_e32 vcc, v173, v186
	s_nop 0
	v_cndmask_b32_e64 v168, 0, 1, s[16:17]
	v_addc_co_u32_e32 v167, vcc, v167, v168, vcc
	v_cmp_gt_f32_e32 vcc, v174, v186
	s_nop 1
	v_cndmask_b32_e64 v168, 0, 1, vcc
	v_cmp_gt_f32_e32 vcc, v175, v186
	ds_read_b128 v[172:175], v154 offset:528
	s_nop 0
	v_addc_co_u32_e32 v167, vcc, v167, v168, vcc
	ds_read_b128 v[168:171], v154 offset:512
	v_cmp_gt_u32_e32 vcc, 16, v167
	v_add_u32_e32 v167, 16, v167
	s_and_b64 vcc, s[4:5], vcc
	v_cndmask_b32_e32 v167, v151, v167, vcc
	v_lshlrev_b32_e32 v167, 2, v167
	s_waitcnt lgkmcnt(0)
	v_cmp_gt_f32_e32 vcc, v169, v165
	ds_permute_b32 v179, v167, v166
	ds_permute_b32 v178, v167, v186
	v_cndmask_b32_e64 v166, 0, 1, vcc
	v_cmp_gt_f32_e32 vcc, v168, v165
	s_nop 1
	v_addc_co_u32_e32 v166, vcc, 0, v166, vcc
	v_cmp_gt_f32_e64 s[16:17], v170, v165
	v_cmp_gt_f32_e32 vcc, v171, v165
	v_cmp_gt_f32_e64 s[98:99], v172, v165
	v_cndmask_b32_e64 v167, 0, 1, s[16:17]
	v_addc_co_u32_e32 v166, vcc, v166, v167, vcc
	v_cmp_gt_f32_e32 vcc, v173, v165
	v_cndmask_b32_e64 v167, 0, 1, s[98:99]
	s_nop 0
	v_addc_co_u32_e32 v170, vcc, v166, v167, vcc
	ds_read_b128 v[166:169], v154 offset:544
	v_cmp_gt_f32_e64 s[16:17], v174, v165
	v_cmp_gt_f32_e32 vcc, v175, v165
	s_nop 0
	v_cndmask_b32_e64 v171, 0, 1, s[16:17]
	v_addc_co_u32_e32 v174, vcc, v170, v171, vcc
	ds_read_b128 v[170:173], v154 offset:560
	s_waitcnt lgkmcnt(1)
	v_cmp_gt_f32_e64 s[16:17], v166, v165
	v_cmp_gt_f32_e32 vcc, v167, v165
	v_cmp_gt_f32_e64 s[98:99], v168, v165
	v_cndmask_b32_e64 v166, 0, 1, s[16:17]
	v_addc_co_u32_e32 v166, vcc, v174, v166, vcc
	v_cmp_gt_f32_e32 vcc, v169, v165
	v_cndmask_b32_e64 v167, 0, 1, s[98:99]
	s_nop 0
	v_addc_co_u32_e32 v166, vcc, v166, v167, vcc
	s_waitcnt lgkmcnt(0)
	v_cmp_gt_f32_e64 s[16:17], v170, v165
	v_cmp_gt_f32_e32 vcc, v171, v165
	s_nop 0
	v_cndmask_b32_e64 v167, 0, 1, s[16:17]
	v_addc_co_u32_e32 v170, vcc, v166, v167, vcc
	ds_read_b128 v[166:169], v154 offset:576
	v_cmp_gt_f32_e64 s[16:17], v172, v165
	v_cmp_gt_f32_e32 vcc, v173, v165
	s_nop 0
	v_cndmask_b32_e64 v171, 0, 1, s[16:17]
	v_addc_co_u32_e32 v174, vcc, v170, v171, vcc
	ds_read_b128 v[170:173], v154 offset:592
	s_waitcnt lgkmcnt(1)
	v_cmp_gt_f32_e64 s[16:17], v166, v165
	v_cmp_gt_f32_e32 vcc, v167, v165
	v_cmp_gt_f32_e64 s[98:99], v168, v165
	v_cndmask_b32_e64 v166, 0, 1, s[16:17]
	v_addc_co_u32_e32 v166, vcc, v174, v166, vcc
	v_cmp_gt_f32_e32 vcc, v169, v165
	v_cndmask_b32_e64 v167, 0, 1, s[98:99]
	s_nop 0
	v_addc_co_u32_e32 v166, vcc, v166, v167, vcc
	s_waitcnt lgkmcnt(0)
	v_cmp_gt_f32_e64 s[16:17], v170, v165
	v_cmp_gt_f32_e32 vcc, v171, v165
	s_nop 0
	v_cndmask_b32_e64 v167, 0, 1, s[16:17]
	v_addc_co_u32_e32 v170, vcc, v166, v167, vcc
	ds_read_b128 v[166:169], v154 offset:608
	v_cmp_gt_f32_e64 s[16:17], v172, v165
	v_cmp_gt_f32_e32 vcc, v173, v165
	s_nop 0
	v_cndmask_b32_e64 v171, 0, 1, s[16:17]
	v_addc_co_u32_e32 v174, vcc, v170, v171, vcc
	ds_read_b128 v[170:173], v154 offset:624
	s_waitcnt lgkmcnt(1)
	v_cmp_gt_f32_e64 s[16:17], v166, v165
	v_cmp_gt_f32_e32 vcc, v167, v165
	v_cmp_gt_f32_e64 s[98:99], v168, v165
	v_cndmask_b32_e64 v166, 0, 1, s[16:17]
	v_addc_co_u32_e32 v166, vcc, v174, v166, vcc
	v_cmp_gt_f32_e32 vcc, v169, v165
	v_cndmask_b32_e64 v167, 0, 1, s[98:99]
	s_nop 0
	v_addc_co_u32_e32 v166, vcc, v166, v167, vcc
	s_waitcnt lgkmcnt(0)
	v_cmp_gt_f32_e64 s[16:17], v170, v165
	v_cmp_gt_f32_e32 vcc, v171, v165
	s_nop 0
	v_cndmask_b32_e64 v167, 0, 1, s[16:17]
	v_addc_co_u32_e32 v170, vcc, v166, v167, vcc
	ds_read_b128 v[166:169], v154 offset:640
	v_cmp_gt_f32_e64 s[16:17], v172, v165
	v_cmp_gt_f32_e32 vcc, v173, v165
	s_nop 0
	v_cndmask_b32_e64 v171, 0, 1, s[16:17]
	v_addc_co_u32_e32 v174, vcc, v170, v171, vcc
	ds_read_b128 v[170:173], v154 offset:656
	s_waitcnt lgkmcnt(1)
	v_cmp_gt_f32_e64 s[16:17], v166, v165
	v_cmp_gt_f32_e32 vcc, v167, v165
	v_cmp_gt_f32_e64 s[98:99], v168, v165
	v_cndmask_b32_e64 v166, 0, 1, s[16:17]
	v_addc_co_u32_e32 v166, vcc, v174, v166, vcc
	v_cmp_gt_f32_e32 vcc, v169, v165
	v_cndmask_b32_e64 v167, 0, 1, s[98:99]
	s_nop 0
	v_addc_co_u32_e32 v166, vcc, v166, v167, vcc
	s_waitcnt lgkmcnt(0)
	v_cmp_gt_f32_e64 s[16:17], v170, v165
	v_cmp_gt_f32_e32 vcc, v171, v165
	s_nop 0
	v_cndmask_b32_e64 v167, 0, 1, s[16:17]
	v_addc_co_u32_e32 v170, vcc, v166, v167, vcc
	ds_read_b128 v[166:169], v154 offset:672
	v_cmp_gt_f32_e64 s[16:17], v172, v165
	v_cmp_gt_f32_e32 vcc, v173, v165
	s_nop 0
	v_cndmask_b32_e64 v171, 0, 1, s[16:17]
	v_addc_co_u32_e32 v174, vcc, v170, v171, vcc
	ds_read_b128 v[170:173], v154 offset:688
	s_waitcnt lgkmcnt(1)
	v_cmp_gt_f32_e64 s[16:17], v166, v165
	v_cmp_gt_f32_e32 vcc, v167, v165
	v_cmp_gt_f32_e64 s[98:99], v168, v165
	v_cndmask_b32_e64 v166, 0, 1, s[16:17]
	v_addc_co_u32_e32 v166, vcc, v174, v166, vcc
	v_cmp_gt_f32_e32 vcc, v169, v165
	v_cndmask_b32_e64 v167, 0, 1, s[98:99]
	s_nop 0
	v_addc_co_u32_e32 v166, vcc, v166, v167, vcc
	s_waitcnt lgkmcnt(0)
	v_cmp_gt_f32_e64 s[16:17], v170, v165
	v_cmp_gt_f32_e32 vcc, v171, v165
	s_nop 0
	v_cndmask_b32_e64 v167, 0, 1, s[16:17]
	v_addc_co_u32_e32 v170, vcc, v166, v167, vcc
	ds_read_b128 v[166:169], v154 offset:704
	v_cmp_gt_f32_e64 s[16:17], v172, v165
	v_cmp_gt_f32_e32 vcc, v173, v165
	s_nop 0
	v_cndmask_b32_e64 v171, 0, 1, s[16:17]
	v_addc_co_u32_e32 v174, vcc, v170, v171, vcc
	ds_read_b128 v[170:173], v154 offset:768
	s_waitcnt lgkmcnt(1)
	v_cmp_gt_f32_e64 s[16:17], v166, v165
	v_cmp_gt_f32_e32 vcc, v167, v165
	s_nop 0
	v_cndmask_b32_e64 v166, 0, 1, s[16:17]
	v_addc_co_u32_e32 v166, vcc, v174, v166, vcc
	v_cmp_gt_f32_e32 vcc, v168, v165
	v_cndmask_b32_e64 v168, v177, v178, s[46:47]
	s_nop 0
	v_cndmask_b32_e64 v167, 0, 1, vcc
	v_cmp_gt_f32_e32 vcc, v169, v165
	s_nop 1
	v_addc_co_u32_e32 v166, vcc, v166, v167, vcc
	v_cmp_gt_u32_e32 vcc, 16, v166
	v_add_u32_e32 v166, 32, v166
	s_and_b64 vcc, s[4:5], vcc
	v_cndmask_b32_e32 v166, v152, v166, vcc
	v_lshlrev_b32_e32 v166, 2, v166
	ds_permute_b32 v165, v166, v165
	s_waitcnt lgkmcnt(1)
	v_cmp_gt_f32_e32 vcc, v171, v163
	v_cndmask_b32_e64 v167, 0, v176, s[44:45]
	ds_permute_b32 v175, v166, v164
	v_cndmask_b32_e64 v164, 0, 1, vcc
	v_cmp_gt_f32_e32 vcc, v170, v163
	v_cndmask_b32_e64 v174, v167, v179, s[46:47]
	s_waitcnt lgkmcnt(1)
	v_cndmask_b32_e64 v176, v168, v165, s[48:49]
	v_addc_co_u32_e32 v168, vcc, 0, v164, vcc
	ds_read_b128 v[164:167], v154 offset:784
	v_cmp_gt_f32_e64 s[16:17], v172, v163
	v_cmp_gt_f32_e32 vcc, v173, v163
	s_nop 0
	v_cndmask_b32_e64 v169, 0, 1, s[16:17]
	v_addc_co_u32_e32 v172, vcc, v168, v169, vcc
	ds_read_b128 v[168:171], v154 offset:800
	s_waitcnt lgkmcnt(1)
	v_cmp_gt_f32_e64 s[16:17], v164, v163
	v_cmp_gt_f32_e32 vcc, v165, v163
	v_cmp_gt_f32_e64 s[98:99], v166, v163
	v_cndmask_b32_e64 v164, 0, 1, s[16:17]
	v_addc_co_u32_e32 v164, vcc, v172, v164, vcc
	v_cmp_gt_f32_e32 vcc, v167, v163
	v_cndmask_b32_e64 v165, 0, 1, s[98:99]
	s_nop 0
	v_addc_co_u32_e32 v164, vcc, v164, v165, vcc
	s_waitcnt lgkmcnt(0)
	v_cmp_gt_f32_e64 s[16:17], v168, v163
	v_cmp_gt_f32_e32 vcc, v169, v163
	s_nop 0
	v_cndmask_b32_e64 v165, 0, 1, s[16:17]
	v_addc_co_u32_e32 v168, vcc, v164, v165, vcc
	ds_read_b128 v[164:167], v154 offset:816
	v_cmp_gt_f32_e64 s[16:17], v170, v163
	v_cmp_gt_f32_e32 vcc, v171, v163
	s_nop 0
	v_cndmask_b32_e64 v169, 0, 1, s[16:17]
	v_addc_co_u32_e32 v172, vcc, v168, v169, vcc
	ds_read_b128 v[168:171], v154 offset:832
	s_waitcnt lgkmcnt(1)
	v_cmp_gt_f32_e64 s[16:17], v164, v163
	v_cmp_gt_f32_e32 vcc, v165, v163
	v_cmp_gt_f32_e64 s[98:99], v166, v163
	v_cndmask_b32_e64 v164, 0, 1, s[16:17]
	v_addc_co_u32_e32 v164, vcc, v172, v164, vcc
	v_cmp_gt_f32_e32 vcc, v167, v163
	v_cndmask_b32_e64 v165, 0, 1, s[98:99]
	s_nop 0
	v_addc_co_u32_e32 v164, vcc, v164, v165, vcc
	s_waitcnt lgkmcnt(0)
	v_cmp_gt_f32_e64 s[16:17], v168, v163
	v_cmp_gt_f32_e32 vcc, v169, v163
	s_nop 0
	v_cndmask_b32_e64 v165, 0, 1, s[16:17]
	v_addc_co_u32_e32 v168, vcc, v164, v165, vcc
	ds_read_b128 v[164:167], v154 offset:848
	v_cmp_gt_f32_e64 s[16:17], v170, v163
	v_cmp_gt_f32_e32 vcc, v171, v163
	s_nop 0
	v_cndmask_b32_e64 v169, 0, 1, s[16:17]
	v_addc_co_u32_e32 v172, vcc, v168, v169, vcc
	ds_read_b128 v[168:171], v154 offset:864
	s_waitcnt lgkmcnt(1)
	v_cmp_gt_f32_e64 s[16:17], v164, v163
	v_cmp_gt_f32_e32 vcc, v165, v163
	v_cmp_gt_f32_e64 s[98:99], v166, v163
	v_cndmask_b32_e64 v164, 0, 1, s[16:17]
	v_addc_co_u32_e32 v164, vcc, v172, v164, vcc
	v_cmp_gt_f32_e32 vcc, v167, v163
	v_cndmask_b32_e64 v165, 0, 1, s[98:99]
	s_nop 0
	v_addc_co_u32_e32 v164, vcc, v164, v165, vcc
	s_waitcnt lgkmcnt(0)
	v_cmp_gt_f32_e64 s[16:17], v168, v163
	v_cmp_gt_f32_e32 vcc, v169, v163
	s_nop 0
	v_cndmask_b32_e64 v165, 0, 1, s[16:17]
	v_addc_co_u32_e32 v168, vcc, v164, v165, vcc
	ds_read_b128 v[164:167], v154 offset:880
	v_cmp_gt_f32_e64 s[16:17], v170, v163
	v_cmp_gt_f32_e32 vcc, v171, v163
	s_nop 0
	v_cndmask_b32_e64 v169, 0, 1, s[16:17]
	v_addc_co_u32_e32 v172, vcc, v168, v169, vcc
	ds_read_b128 v[168:171], v154 offset:896
	s_waitcnt lgkmcnt(1)
	v_cmp_gt_f32_e64 s[16:17], v164, v163
	v_cmp_gt_f32_e32 vcc, v165, v163
	v_cmp_gt_f32_e64 s[98:99], v166, v163
	v_cndmask_b32_e64 v164, 0, 1, s[16:17]
	v_addc_co_u32_e32 v164, vcc, v172, v164, vcc
	v_cmp_gt_f32_e32 vcc, v167, v163
	v_cndmask_b32_e64 v165, 0, 1, s[98:99]
	s_nop 0
	v_addc_co_u32_e32 v164, vcc, v164, v165, vcc
	s_waitcnt lgkmcnt(0)
	v_cmp_gt_f32_e64 s[16:17], v168, v163
	v_cmp_gt_f32_e32 vcc, v169, v163
	s_nop 0
	v_cndmask_b32_e64 v165, 0, 1, s[16:17]
	v_addc_co_u32_e32 v168, vcc, v164, v165, vcc
	ds_read_b128 v[164:167], v154 offset:912
	v_cmp_gt_f32_e64 s[16:17], v170, v163
	v_cmp_gt_f32_e32 vcc, v171, v163
	s_nop 0
	v_cndmask_b32_e64 v169, 0, 1, s[16:17]
	v_addc_co_u32_e32 v172, vcc, v168, v169, vcc
	ds_read_b128 v[168:171], v154 offset:928
	s_waitcnt lgkmcnt(1)
	v_cmp_gt_f32_e64 s[16:17], v164, v163
	v_cmp_gt_f32_e32 vcc, v165, v163
	v_cmp_gt_f32_e64 s[98:99], v166, v163
	v_cndmask_b32_e64 v164, 0, 1, s[16:17]
	v_addc_co_u32_e32 v164, vcc, v172, v164, vcc
	v_cmp_gt_f32_e32 vcc, v167, v163
	v_cndmask_b32_e64 v165, 0, 1, s[98:99]
	s_nop 0
	v_addc_co_u32_e32 v164, vcc, v164, v165, vcc
	s_waitcnt lgkmcnt(0)
	v_cmp_gt_f32_e64 s[16:17], v168, v163
	v_cmp_gt_f32_e32 vcc, v169, v163
	s_nop 0
	v_cndmask_b32_e64 v165, 0, 1, s[16:17]
	v_addc_co_u32_e32 v168, vcc, v164, v165, vcc
	ds_read_b128 v[164:167], v154 offset:944
	v_cmp_gt_f32_e64 s[16:17], v170, v163
	v_cmp_gt_f32_e32 vcc, v171, v163
	s_nop 0
	v_cndmask_b32_e64 v169, 0, 1, s[16:17]
	v_addc_co_u32_e32 v172, vcc, v168, v169, vcc
	ds_read_b128 v[168:171], v154 offset:960
	s_waitcnt lgkmcnt(1)
	v_cmp_gt_f32_e64 s[16:17], v164, v163
	v_cmp_gt_f32_e32 vcc, v165, v163
	v_cmp_gt_f32_e64 s[98:99], v166, v163
	v_cndmask_b32_e64 v164, 0, 1, s[16:17]
	v_addc_co_u32_e32 v164, vcc, v172, v164, vcc
	v_cmp_gt_f32_e32 vcc, v167, v163
	v_cndmask_b32_e64 v165, 0, 1, s[98:99]
	s_nop 0
	v_addc_co_u32_e32 v164, vcc, v164, v165, vcc
	s_waitcnt lgkmcnt(0)
	v_cmp_gt_f32_e64 s[16:17], v168, v163
	v_cmp_gt_f32_e32 vcc, v169, v163
	v_cmp_gt_f32_e64 s[98:99], v170, v163
	v_cndmask_b32_e64 v165, 0, 1, s[16:17]
	v_addc_co_u32_e32 v164, vcc, v164, v165, vcc
	v_cmp_gt_f32_e32 vcc, v171, v163
	v_cndmask_b32_e64 v165, 0, 1, s[98:99]
	s_nop 0
	v_addc_co_u32_e32 v164, vcc, v164, v165, vcc
	v_cmp_gt_u32_e32 vcc, 16, v164
	v_add_u32_e32 v164, 48, v164
	s_and_b64 vcc, s[4:5], vcc
	v_cndmask_b32_e32 v168, v140, v164, vcc
	ds_read_b128 v[164:167], v154 offset:1024
	v_lshlrev_b32_e32 v168, 2, v168
	ds_permute_b32 v172, v168, v163
	ds_permute_b32 v173, v168, v162
	ds_read_b128 v[168:171], v154 offset:1040
	s_waitcnt lgkmcnt(3)
	v_cmp_gt_f32_e64 s[16:17], v165, v161
	v_cmp_gt_f32_e32 vcc, v164, v161
	v_cmp_gt_f32_e64 s[98:99], v166, v161
	v_cndmask_b32_e64 v162, 0, 1, s[16:17]
	v_addc_co_u32_e32 v162, vcc, 0, v162, vcc
	v_cmp_gt_f32_e32 vcc, v167, v161
	v_cndmask_b32_e64 v163, 0, 1, s[98:99]
	s_nop 0
	v_addc_co_u32_e32 v162, vcc, v162, v163, vcc
	s_waitcnt lgkmcnt(0)
	v_cmp_gt_f32_e64 s[16:17], v168, v161
	v_cmp_gt_f32_e32 vcc, v169, v161
	s_nop 0
	v_cndmask_b32_e64 v163, 0, 1, s[16:17]
	v_addc_co_u32_e32 v166, vcc, v162, v163, vcc
	ds_read_b128 v[162:165], v154 offset:1056
	v_cmp_gt_f32_e64 s[16:17], v170, v161
	v_cmp_gt_f32_e32 vcc, v171, v161
	s_nop 0
	v_cndmask_b32_e64 v167, 0, 1, s[16:17]
	v_addc_co_u32_e32 v170, vcc, v166, v167, vcc
	ds_read_b128 v[166:169], v154 offset:1072
	s_waitcnt lgkmcnt(1)
	v_cmp_gt_f32_e64 s[16:17], v162, v161
	v_cmp_gt_f32_e32 vcc, v163, v161
	v_cmp_gt_f32_e64 s[98:99], v164, v161
	v_cndmask_b32_e64 v162, 0, 1, s[16:17]
	v_addc_co_u32_e32 v162, vcc, v170, v162, vcc
	v_cmp_gt_f32_e32 vcc, v165, v161
	v_cndmask_b32_e64 v163, 0, 1, s[98:99]
	s_nop 0
	v_addc_co_u32_e32 v162, vcc, v162, v163, vcc
	s_waitcnt lgkmcnt(0)
	v_cmp_gt_f32_e64 s[16:17], v166, v161
	v_cmp_gt_f32_e32 vcc, v167, v161
	s_nop 0
	v_cndmask_b32_e64 v163, 0, 1, s[16:17]
	v_addc_co_u32_e32 v166, vcc, v162, v163, vcc
	ds_read_b128 v[162:165], v154 offset:1088
	v_cmp_gt_f32_e64 s[16:17], v168, v161
	v_cmp_gt_f32_e32 vcc, v169, v161
	s_nop 0
	v_cndmask_b32_e64 v167, 0, 1, s[16:17]
	v_addc_co_u32_e32 v170, vcc, v166, v167, vcc
	ds_read_b128 v[166:169], v154 offset:1104
	s_waitcnt lgkmcnt(1)
	v_cmp_gt_f32_e64 s[16:17], v162, v161
	v_cmp_gt_f32_e32 vcc, v163, v161
	v_cmp_gt_f32_e64 s[98:99], v164, v161
	v_cndmask_b32_e64 v162, 0, 1, s[16:17]
	v_addc_co_u32_e32 v162, vcc, v170, v162, vcc
	v_cmp_gt_f32_e32 vcc, v165, v161
	v_cndmask_b32_e64 v163, 0, 1, s[98:99]
	s_nop 0
	v_addc_co_u32_e32 v162, vcc, v162, v163, vcc
	s_waitcnt lgkmcnt(0)
	v_cmp_gt_f32_e64 s[16:17], v166, v161
	v_cmp_gt_f32_e32 vcc, v167, v161
	s_nop 0
	v_cndmask_b32_e64 v163, 0, 1, s[16:17]
	v_addc_co_u32_e32 v166, vcc, v162, v163, vcc
	ds_read_b128 v[162:165], v154 offset:1120
	v_cmp_gt_f32_e64 s[16:17], v168, v161
	v_cmp_gt_f32_e32 vcc, v169, v161
	s_nop 0
	v_cndmask_b32_e64 v167, 0, 1, s[16:17]
	v_addc_co_u32_e32 v170, vcc, v166, v167, vcc
	ds_read_b128 v[166:169], v154 offset:1136
	s_waitcnt lgkmcnt(1)
	v_cmp_gt_f32_e64 s[16:17], v162, v161
	v_cmp_gt_f32_e32 vcc, v163, v161
	v_cmp_gt_f32_e64 s[98:99], v164, v161
	v_cndmask_b32_e64 v162, 0, 1, s[16:17]
	v_addc_co_u32_e32 v162, vcc, v170, v162, vcc
	v_cmp_gt_f32_e32 vcc, v165, v161
	v_cndmask_b32_e64 v163, 0, 1, s[98:99]
	s_nop 0
	v_addc_co_u32_e32 v162, vcc, v162, v163, vcc
	s_waitcnt lgkmcnt(0)
	v_cmp_gt_f32_e64 s[16:17], v166, v161
	v_cmp_gt_f32_e32 vcc, v167, v161
	s_nop 0
	v_cndmask_b32_e64 v163, 0, 1, s[16:17]
	v_addc_co_u32_e32 v166, vcc, v162, v163, vcc
	ds_read_b128 v[162:165], v154 offset:1152
	v_cmp_gt_f32_e64 s[16:17], v168, v161
	v_cmp_gt_f32_e32 vcc, v169, v161
	s_nop 0
	v_cndmask_b32_e64 v167, 0, 1, s[16:17]
	v_addc_co_u32_e32 v170, vcc, v166, v167, vcc
	ds_read_b128 v[166:169], v154 offset:1168
	s_waitcnt lgkmcnt(1)
	v_cmp_gt_f32_e64 s[16:17], v162, v161
	v_cmp_gt_f32_e32 vcc, v163, v161
	v_cmp_gt_f32_e64 s[98:99], v164, v161
	v_cndmask_b32_e64 v162, 0, 1, s[16:17]
	v_addc_co_u32_e32 v162, vcc, v170, v162, vcc
	v_cmp_gt_f32_e32 vcc, v165, v161
	v_cndmask_b32_e64 v163, 0, 1, s[98:99]
	s_nop 0
	v_addc_co_u32_e32 v162, vcc, v162, v163, vcc
	s_waitcnt lgkmcnt(0)
	v_cmp_gt_f32_e64 s[16:17], v166, v161
	v_cmp_gt_f32_e32 vcc, v167, v161
	s_nop 0
	v_cndmask_b32_e64 v163, 0, 1, s[16:17]
	v_addc_co_u32_e32 v166, vcc, v162, v163, vcc
	ds_read_b128 v[162:165], v154 offset:1184
	v_cmp_gt_f32_e64 s[16:17], v168, v161
	v_cmp_gt_f32_e32 vcc, v169, v161
	s_nop 0
	v_cndmask_b32_e64 v167, 0, 1, s[16:17]
	v_addc_co_u32_e32 v170, vcc, v166, v167, vcc
	ds_read_b128 v[166:169], v154 offset:1200
	s_waitcnt lgkmcnt(1)
	v_cmp_gt_f32_e64 s[16:17], v162, v161
	v_cmp_gt_f32_e32 vcc, v163, v161
	v_cmp_gt_f32_e64 s[98:99], v164, v161
	v_cndmask_b32_e64 v162, 0, 1, s[16:17]
	v_addc_co_u32_e32 v162, vcc, v170, v162, vcc
	v_cmp_gt_f32_e32 vcc, v165, v161
	v_cndmask_b32_e64 v163, 0, 1, s[98:99]
	s_nop 0
	v_addc_co_u32_e32 v162, vcc, v162, v163, vcc
	s_waitcnt lgkmcnt(0)
	v_cmp_gt_f32_e64 s[16:17], v166, v161
	v_cmp_gt_f32_e32 vcc, v167, v161
	s_nop 0
	v_cndmask_b32_e64 v163, 0, 1, s[16:17]
	v_addc_co_u32_e32 v166, vcc, v162, v163, vcc
	ds_read_b128 v[162:165], v154 offset:1216
	v_cmp_gt_f32_e64 s[16:17], v168, v161
	v_cmp_gt_f32_e32 vcc, v169, v161
	s_nop 0
	v_cndmask_b32_e64 v167, 0, 1, s[16:17]
	v_addc_co_u32_e32 v170, vcc, v166, v167, vcc
	ds_read_b128 v[166:169], v154 offset:1280
	s_waitcnt lgkmcnt(1)
	v_cmp_gt_f32_e64 s[16:17], v162, v161
	v_cmp_gt_f32_e32 vcc, v163, v161
	v_cmp_gt_f32_e64 s[98:99], v164, v161
	v_cndmask_b32_e64 v162, 0, 1, s[16:17]
	v_addc_co_u32_e32 v162, vcc, v170, v162, vcc
	v_cmp_gt_f32_e32 vcc, v165, v161
	v_cndmask_b32_e64 v163, 0, 1, s[98:99]
	s_nop 0
	v_addc_co_u32_e32 v162, vcc, v162, v163, vcc
	v_cmp_gt_u32_e32 vcc, 16, v162
	s_and_b64 vcc, s[4:5], vcc
	s_nop 0
	v_cndmask_b32_e32 v162, v150, v162, vcc
	v_lshlrev_b32_e32 v163, 2, v162
	ds_permute_b32 v164, v163, v161
	s_waitcnt lgkmcnt(1)
	v_cmp_gt_f32_e32 vcc, v167, v159
	ds_permute_b32 v160, v163, v160
	v_cndmask_b32_e64 v162, v176, v172, s[50:51]
	v_cndmask_b32_e64 v161, v174, v175, s[48:49]
	s_waitcnt lgkmcnt(1)
	v_cndmask_b32_e64 v163, 0, v164, s[44:45]
	v_cndmask_b32_e64 v164, 0, 1, vcc
	v_cmp_gt_f32_e32 vcc, v166, v159
	s_waitcnt lgkmcnt(0)
	v_cndmask_b32_e64 v160, 0, v160, s[44:45]
	v_cndmask_b32_e64 v161, v161, v173, s[50:51]
	v_addc_co_u32_e32 v170, vcc, 0, v164, vcc
	ds_read_b128 v[164:167], v154 offset:1296
	v_cmp_gt_f32_e32 vcc, v168, v159
	v_lshlrev_b32_e32 v161, 7, v161
	s_nop 0
	v_cndmask_b32_e64 v168, 0, 1, vcc
	v_cmp_gt_f32_e32 vcc, v169, v159
	s_nop 1
	v_addc_co_u32_e32 v172, vcc, v170, v168, vcc
	ds_read_b128 v[168:171], v154 offset:1312
	s_waitcnt lgkmcnt(1)
	v_cmp_gt_f32_e64 s[16:17], v164, v159
	v_cmp_gt_f32_e32 vcc, v165, v159
	v_cmp_gt_f32_e64 s[98:99], v166, v159
	v_cndmask_b32_e64 v164, 0, 1, s[16:17]
	v_addc_co_u32_e32 v164, vcc, v172, v164, vcc
	v_cmp_gt_f32_e32 vcc, v167, v159
	v_cndmask_b32_e64 v165, 0, 1, s[98:99]
	s_nop 0
	v_addc_co_u32_e32 v164, vcc, v164, v165, vcc
	s_waitcnt lgkmcnt(0)
	v_cmp_gt_f32_e64 s[16:17], v168, v159
	v_cmp_gt_f32_e32 vcc, v169, v159
	s_nop 0
	v_cndmask_b32_e64 v165, 0, 1, s[16:17]
	v_addc_co_u32_e32 v168, vcc, v164, v165, vcc
	ds_read_b128 v[164:167], v154 offset:1328
	v_cmp_gt_f32_e64 s[16:17], v170, v159
	v_cmp_gt_f32_e32 vcc, v171, v159
	s_nop 0
	v_cndmask_b32_e64 v169, 0, 1, s[16:17]
	v_addc_co_u32_e32 v172, vcc, v168, v169, vcc
	ds_read_b128 v[168:171], v154 offset:1344
	s_waitcnt lgkmcnt(1)
	v_cmp_gt_f32_e64 s[16:17], v164, v159
	v_cmp_gt_f32_e32 vcc, v165, v159
	v_cmp_gt_f32_e64 s[98:99], v166, v159
	v_cndmask_b32_e64 v164, 0, 1, s[16:17]
	v_addc_co_u32_e32 v164, vcc, v172, v164, vcc
	v_cmp_gt_f32_e32 vcc, v167, v159
	v_cndmask_b32_e64 v165, 0, 1, s[98:99]
	s_nop 0
	v_addc_co_u32_e32 v164, vcc, v164, v165, vcc
	s_waitcnt lgkmcnt(0)
	v_cmp_gt_f32_e64 s[16:17], v168, v159
	v_cmp_gt_f32_e32 vcc, v169, v159
	s_nop 0
	v_cndmask_b32_e64 v165, 0, 1, s[16:17]
	v_addc_co_u32_e32 v168, vcc, v164, v165, vcc
	ds_read_b128 v[164:167], v154 offset:1360
	v_cmp_gt_f32_e64 s[16:17], v170, v159
	v_cmp_gt_f32_e32 vcc, v171, v159
	s_nop 0
	v_cndmask_b32_e64 v169, 0, 1, s[16:17]
	v_addc_co_u32_e32 v172, vcc, v168, v169, vcc
	ds_read_b128 v[168:171], v154 offset:1376
	s_waitcnt lgkmcnt(1)
	v_cmp_gt_f32_e64 s[16:17], v164, v159
	v_cmp_gt_f32_e32 vcc, v165, v159
	v_cmp_gt_f32_e64 s[98:99], v166, v159
	v_cndmask_b32_e64 v164, 0, 1, s[16:17]
	v_addc_co_u32_e32 v164, vcc, v172, v164, vcc
	v_cmp_gt_f32_e32 vcc, v167, v159
	v_cndmask_b32_e64 v165, 0, 1, s[98:99]
	s_nop 0
	v_addc_co_u32_e32 v164, vcc, v164, v165, vcc
	s_waitcnt lgkmcnt(0)
	v_cmp_gt_f32_e64 s[16:17], v168, v159
	v_cmp_gt_f32_e32 vcc, v169, v159
	s_nop 0
	v_cndmask_b32_e64 v165, 0, 1, s[16:17]
	v_addc_co_u32_e32 v168, vcc, v164, v165, vcc
	ds_read_b128 v[164:167], v154 offset:1392
	v_cmp_gt_f32_e64 s[16:17], v170, v159
	v_cmp_gt_f32_e32 vcc, v171, v159
	s_nop 0
	v_cndmask_b32_e64 v169, 0, 1, s[16:17]
	v_addc_co_u32_e32 v172, vcc, v168, v169, vcc
	ds_read_b128 v[168:171], v154 offset:1408
	s_waitcnt lgkmcnt(1)
	v_cmp_gt_f32_e64 s[16:17], v164, v159
	v_cmp_gt_f32_e32 vcc, v165, v159
	v_cmp_gt_f32_e64 s[98:99], v166, v159
	v_cndmask_b32_e64 v164, 0, 1, s[16:17]
	v_addc_co_u32_e32 v164, vcc, v172, v164, vcc
	v_cmp_gt_f32_e32 vcc, v167, v159
	v_cndmask_b32_e64 v165, 0, 1, s[98:99]
	s_nop 0
	v_addc_co_u32_e32 v164, vcc, v164, v165, vcc
	s_waitcnt lgkmcnt(0)
	v_cmp_gt_f32_e64 s[16:17], v168, v159
	v_cmp_gt_f32_e32 vcc, v169, v159
	s_nop 0
	v_cndmask_b32_e64 v165, 0, 1, s[16:17]
	v_addc_co_u32_e32 v168, vcc, v164, v165, vcc
	ds_read_b128 v[164:167], v154 offset:1424
	v_cmp_gt_f32_e64 s[16:17], v170, v159
	v_cmp_gt_f32_e32 vcc, v171, v159
	s_nop 0
	v_cndmask_b32_e64 v169, 0, 1, s[16:17]
	v_addc_co_u32_e32 v172, vcc, v168, v169, vcc
	ds_read_b128 v[168:171], v154 offset:1440
	s_waitcnt lgkmcnt(1)
	v_cmp_gt_f32_e64 s[16:17], v164, v159
	v_cmp_gt_f32_e32 vcc, v165, v159
	v_cmp_gt_f32_e64 s[98:99], v166, v159
	v_cndmask_b32_e64 v164, 0, 1, s[16:17]
	v_addc_co_u32_e32 v164, vcc, v172, v164, vcc
	v_cmp_gt_f32_e32 vcc, v167, v159
	v_cndmask_b32_e64 v165, 0, 1, s[98:99]
	s_nop 0
	v_addc_co_u32_e32 v164, vcc, v164, v165, vcc
	s_waitcnt lgkmcnt(0)
	v_cmp_gt_f32_e64 s[16:17], v168, v159
	v_cmp_gt_f32_e32 vcc, v169, v159
	s_nop 0
	v_cndmask_b32_e64 v165, 0, 1, s[16:17]
	v_addc_co_u32_e32 v168, vcc, v164, v165, vcc
	ds_read_b128 v[164:167], v154 offset:1456
	v_cmp_gt_f32_e64 s[16:17], v170, v159
	v_cmp_gt_f32_e32 vcc, v171, v159
	s_nop 0
	v_cndmask_b32_e64 v169, 0, 1, s[16:17]
	v_addc_co_u32_e32 v172, vcc, v168, v169, vcc
	ds_read_b128 v[168:171], v154 offset:1472
	s_waitcnt lgkmcnt(1)
	v_cmp_gt_f32_e64 s[16:17], v164, v159
	v_cmp_gt_f32_e32 vcc, v165, v159
	v_cmp_gt_f32_e64 s[98:99], v166, v159
	v_cndmask_b32_e64 v164, 0, 1, s[16:17]
	v_addc_co_u32_e32 v164, vcc, v172, v164, vcc
	v_cmp_gt_f32_e32 vcc, v167, v159
	v_cndmask_b32_e64 v165, 0, 1, s[98:99]
	s_nop 0
	v_addc_co_u32_e32 v164, vcc, v164, v165, vcc
	s_waitcnt lgkmcnt(0)
	v_cmp_gt_f32_e64 s[16:17], v168, v159
	v_cmp_gt_f32_e32 vcc, v169, v159
	v_cmp_gt_f32_e64 s[98:99], v170, v159
	v_cndmask_b32_e64 v165, 0, 1, s[16:17]
	v_addc_co_u32_e32 v164, vcc, v164, v165, vcc
	v_cmp_gt_f32_e32 vcc, v171, v159
	v_cndmask_b32_e64 v165, 0, 1, s[98:99]
	s_nop 0
	v_addc_co_u32_e32 v164, vcc, v164, v165, vcc
	v_cmp_gt_u32_e32 vcc, 16, v164
	v_add_u32_e32 v164, 16, v164
	s_and_b64 vcc, s[4:5], vcc
	v_cndmask_b32_e32 v168, v151, v164, vcc
	ds_read_b128 v[164:167], v154 offset:1536
	v_lshlrev_b32_e32 v168, 2, v168
	ds_permute_b32 v159, v168, v159
	ds_permute_b32 v158, v168, v158
	ds_read_b128 v[168:171], v154 offset:1552
	s_waitcnt lgkmcnt(3)
	v_cmp_gt_f32_e32 vcc, v165, v157
	s_waitcnt lgkmcnt(2)
	v_cndmask_b32_e64 v159, v163, v159, s[46:47]
	v_cndmask_b32_e64 v165, 0, 1, vcc
	v_cmp_gt_f32_e32 vcc, v164, v157
	s_waitcnt lgkmcnt(1)
	v_cndmask_b32_e64 v158, v160, v158, s[46:47]
	v_addc_co_u32_e32 v164, vcc, 0, v165, vcc
	v_cmp_gt_f32_e64 s[16:17], v166, v157
	v_cmp_gt_f32_e32 vcc, v167, v157
	s_nop 0
	v_cndmask_b32_e64 v165, 0, 1, s[16:17]
	v_addc_co_u32_e32 v164, vcc, v164, v165, vcc
	s_waitcnt lgkmcnt(0)
	v_cmp_gt_f32_e64 s[16:17], v168, v157
	v_cmp_gt_f32_e32 vcc, v169, v157
	s_nop 0
	v_cndmask_b32_e64 v165, 0, 1, s[16:17]
	v_addc_co_u32_e32 v168, vcc, v164, v165, vcc
	ds_read_b128 v[164:167], v154 offset:1568
	v_cmp_gt_f32_e64 s[16:17], v170, v157
	v_cmp_gt_f32_e32 vcc, v171, v157
	s_nop 0
	v_cndmask_b32_e64 v169, 0, 1, s[16:17]
	v_addc_co_u32_e32 v172, vcc, v168, v169, vcc
	ds_read_b128 v[168:171], v154 offset:1584
	s_waitcnt lgkmcnt(1)
	v_cmp_gt_f32_e64 s[16:17], v164, v157
	v_cmp_gt_f32_e32 vcc, v165, v157
	v_cmp_gt_f32_e64 s[98:99], v166, v157
	v_cndmask_b32_e64 v164, 0, 1, s[16:17]
	v_addc_co_u32_e32 v164, vcc, v172, v164, vcc
	v_cmp_gt_f32_e32 vcc, v167, v157
	v_cndmask_b32_e64 v165, 0, 1, s[98:99]
	s_nop 0
	v_addc_co_u32_e32 v164, vcc, v164, v165, vcc
	s_waitcnt lgkmcnt(0)
	v_cmp_gt_f32_e64 s[16:17], v168, v157
	v_cmp_gt_f32_e32 vcc, v169, v157
	s_nop 0
	v_cndmask_b32_e64 v165, 0, 1, s[16:17]
	v_addc_co_u32_e32 v168, vcc, v164, v165, vcc
	ds_read_b128 v[164:167], v154 offset:1600
	v_cmp_gt_f32_e64 s[16:17], v170, v157
	v_cmp_gt_f32_e32 vcc, v171, v157
	s_nop 0
	v_cndmask_b32_e64 v169, 0, 1, s[16:17]
	v_addc_co_u32_e32 v172, vcc, v168, v169, vcc
	ds_read_b128 v[168:171], v154 offset:1616
	s_waitcnt lgkmcnt(1)
	v_cmp_gt_f32_e64 s[16:17], v164, v157
	v_cmp_gt_f32_e32 vcc, v165, v157
	v_cmp_gt_f32_e64 s[98:99], v166, v157
	v_cndmask_b32_e64 v164, 0, 1, s[16:17]
	v_addc_co_u32_e32 v164, vcc, v172, v164, vcc
	v_cmp_gt_f32_e32 vcc, v167, v157
	v_cndmask_b32_e64 v165, 0, 1, s[98:99]
	s_nop 0
	v_addc_co_u32_e32 v164, vcc, v164, v165, vcc
	s_waitcnt lgkmcnt(0)
	v_cmp_gt_f32_e64 s[16:17], v168, v157
	v_cmp_gt_f32_e32 vcc, v169, v157
	s_nop 0
	v_cndmask_b32_e64 v165, 0, 1, s[16:17]
	v_addc_co_u32_e32 v168, vcc, v164, v165, vcc
	ds_read_b128 v[164:167], v154 offset:1632
	v_cmp_gt_f32_e64 s[16:17], v170, v157
	v_cmp_gt_f32_e32 vcc, v171, v157
	s_nop 0
	v_cndmask_b32_e64 v169, 0, 1, s[16:17]
	v_addc_co_u32_e32 v172, vcc, v168, v169, vcc
	ds_read_b128 v[168:171], v154 offset:1648
	s_waitcnt lgkmcnt(1)
	v_cmp_gt_f32_e64 s[16:17], v164, v157
	v_cmp_gt_f32_e32 vcc, v165, v157
	v_cmp_gt_f32_e64 s[98:99], v166, v157
	v_cndmask_b32_e64 v164, 0, 1, s[16:17]
	v_addc_co_u32_e32 v164, vcc, v172, v164, vcc
	v_cmp_gt_f32_e32 vcc, v167, v157
	v_cndmask_b32_e64 v165, 0, 1, s[98:99]
	s_nop 0
	v_addc_co_u32_e32 v164, vcc, v164, v165, vcc
	s_waitcnt lgkmcnt(0)
	v_cmp_gt_f32_e64 s[16:17], v168, v157
	v_cmp_gt_f32_e32 vcc, v169, v157
	s_nop 0
	v_cndmask_b32_e64 v165, 0, 1, s[16:17]
	v_addc_co_u32_e32 v168, vcc, v164, v165, vcc
	ds_read_b128 v[164:167], v154 offset:1664
	v_cmp_gt_f32_e64 s[16:17], v170, v157
	v_cmp_gt_f32_e32 vcc, v171, v157
	s_nop 0
	v_cndmask_b32_e64 v169, 0, 1, s[16:17]
	v_addc_co_u32_e32 v172, vcc, v168, v169, vcc
	ds_read_b128 v[168:171], v154 offset:1680
	s_waitcnt lgkmcnt(1)
	v_cmp_gt_f32_e64 s[16:17], v164, v157
	v_cmp_gt_f32_e32 vcc, v165, v157
	v_cmp_gt_f32_e64 s[98:99], v166, v157
	v_cndmask_b32_e64 v164, 0, 1, s[16:17]
	v_addc_co_u32_e32 v164, vcc, v172, v164, vcc
	v_cmp_gt_f32_e32 vcc, v167, v157
	v_cndmask_b32_e64 v165, 0, 1, s[98:99]
	s_nop 0
	v_addc_co_u32_e32 v164, vcc, v164, v165, vcc
	s_waitcnt lgkmcnt(0)
	v_cmp_gt_f32_e64 s[16:17], v168, v157
	v_cmp_gt_f32_e32 vcc, v169, v157
	s_nop 0
	v_cndmask_b32_e64 v165, 0, 1, s[16:17]
	v_addc_co_u32_e32 v168, vcc, v164, v165, vcc
	ds_read_b128 v[164:167], v154 offset:1696
	v_cmp_gt_f32_e64 s[16:17], v170, v157
	v_cmp_gt_f32_e32 vcc, v171, v157
	s_nop 0
	v_cndmask_b32_e64 v169, 0, 1, s[16:17]
	v_addc_co_u32_e32 v172, vcc, v168, v169, vcc
	ds_read_b128 v[168:171], v154 offset:1712
	s_waitcnt lgkmcnt(1)
	v_cmp_gt_f32_e64 s[16:17], v164, v157
	v_cmp_gt_f32_e32 vcc, v165, v157
	v_cmp_gt_f32_e64 s[98:99], v166, v157
	v_cndmask_b32_e64 v164, 0, 1, s[16:17]
	v_addc_co_u32_e32 v164, vcc, v172, v164, vcc
	v_cmp_gt_f32_e32 vcc, v167, v157
	v_cndmask_b32_e64 v165, 0, 1, s[98:99]
	s_nop 0
	v_addc_co_u32_e32 v164, vcc, v164, v165, vcc
	s_waitcnt lgkmcnt(0)
	v_cmp_gt_f32_e64 s[16:17], v168, v157
	v_cmp_gt_f32_e32 vcc, v169, v157
	s_nop 0
	v_cndmask_b32_e64 v165, 0, 1, s[16:17]
	v_addc_co_u32_e32 v168, vcc, v164, v165, vcc
	ds_read_b128 v[164:167], v154 offset:1728
	v_cmp_gt_f32_e64 s[16:17], v170, v157
	v_cmp_gt_f32_e32 vcc, v171, v157
	s_nop 0
	v_cndmask_b32_e64 v169, 0, 1, s[16:17]
	v_addc_co_u32_e32 v172, vcc, v168, v169, vcc
	ds_read_b128 v[168:171], v154 offset:1792
	s_waitcnt lgkmcnt(1)
	v_cmp_gt_f32_e64 s[16:17], v164, v157
	v_cmp_gt_f32_e32 vcc, v165, v157
	v_cmp_gt_f32_e64 s[98:99], v166, v157
	v_cndmask_b32_e64 v164, 0, 1, s[16:17]
	v_addc_co_u32_e32 v164, vcc, v172, v164, vcc
	v_cmp_gt_f32_e32 vcc, v167, v157
	v_cndmask_b32_e64 v165, 0, 1, s[98:99]
	s_nop 0
	v_addc_co_u32_e32 v164, vcc, v164, v165, vcc
	v_cmp_gt_u32_e32 vcc, 16, v164
	v_add_u32_e32 v164, 32, v164
	s_and_b64 vcc, s[4:5], vcc
	v_cndmask_b32_e32 v164, v152, v164, vcc
	v_lshlrev_b32_e32 v164, 2, v164
	ds_permute_b32 v157, v164, v157
	s_waitcnt lgkmcnt(1)
	v_cmp_gt_f32_e32 vcc, v169, v153
	ds_permute_b32 v155, v164, v155
	ds_read_b128 v[164:167], v154 offset:1808
	s_waitcnt lgkmcnt(2)
	v_cndmask_b32_e64 v157, v159, v157, s[48:49]
	v_cndmask_b32_e64 v159, 0, 1, vcc
	v_cmp_gt_f32_e32 vcc, v168, v153
	s_waitcnt lgkmcnt(1)
	v_cndmask_b32_e64 v155, v158, v155, s[48:49]
	v_addc_co_u32_e32 v159, vcc, 0, v159, vcc
	v_cmp_gt_f32_e32 vcc, v170, v153
	s_nop 1
	v_cndmask_b32_e64 v160, 0, 1, vcc
	v_cmp_gt_f32_e32 vcc, v171, v153
	ds_read_b128 v[168:171], v154 offset:1824
	s_nop 0
	v_addc_co_u32_e32 v159, vcc, v159, v160, vcc
	s_waitcnt lgkmcnt(1)
	v_cmp_gt_f32_e64 s[16:17], v164, v153
	v_cmp_gt_f32_e32 vcc, v165, v153
	s_nop 0
	v_cndmask_b32_e64 v160, 0, 1, s[16:17]
	v_addc_co_u32_e32 v159, vcc, v159, v160, vcc
	v_cmp_gt_f32_e32 vcc, v166, v153
	s_nop 1
	v_cndmask_b32_e64 v160, 0, 1, vcc
	v_cmp_gt_f32_e32 vcc, v167, v153
	ds_read_b128 v[164:167], v154 offset:1840
	s_nop 0
	v_addc_co_u32_e32 v159, vcc, v159, v160, vcc
	s_waitcnt lgkmcnt(1)
	v_cmp_gt_f32_e64 s[16:17], v168, v153
	v_cmp_gt_f32_e32 vcc, v169, v153
	s_nop 0
	v_cndmask_b32_e64 v160, 0, 1, s[16:17]
	v_addc_co_u32_e32 v159, vcc, v159, v160, vcc
	v_cmp_gt_f32_e32 vcc, v170, v153
	s_nop 1
	v_cndmask_b32_e64 v160, 0, 1, vcc
	v_cmp_gt_f32_e32 vcc, v171, v153
	ds_read_b128 v[168:171], v154 offset:1856
	s_nop 0
	v_addc_co_u32_e32 v159, vcc, v159, v160, vcc
	s_waitcnt lgkmcnt(1)
	v_cmp_gt_f32_e64 s[16:17], v164, v153
	v_cmp_gt_f32_e32 vcc, v165, v153
	s_nop 0
	v_cndmask_b32_e64 v160, 0, 1, s[16:17]
	v_addc_co_u32_e32 v159, vcc, v159, v160, vcc
	v_cmp_gt_f32_e32 vcc, v166, v153
	s_nop 1
	v_cndmask_b32_e64 v160, 0, 1, vcc
	v_cmp_gt_f32_e32 vcc, v167, v153
	ds_read_b128 v[164:167], v154 offset:1872
	s_nop 0
	v_addc_co_u32_e32 v159, vcc, v159, v160, vcc
	s_waitcnt lgkmcnt(1)
	v_cmp_gt_f32_e64 s[16:17], v168, v153
	v_cmp_gt_f32_e32 vcc, v169, v153
	s_nop 0
	v_cndmask_b32_e64 v160, 0, 1, s[16:17]
	v_addc_co_u32_e32 v159, vcc, v159, v160, vcc
	v_cmp_gt_f32_e32 vcc, v170, v153
	s_nop 1
	v_cndmask_b32_e64 v160, 0, 1, vcc
	v_cmp_gt_f32_e32 vcc, v171, v153
	ds_read_b128 v[168:171], v154 offset:1888
	s_nop 0
	v_addc_co_u32_e32 v159, vcc, v159, v160, vcc
	s_waitcnt lgkmcnt(1)
	v_cmp_gt_f32_e64 s[16:17], v164, v153
	v_cmp_gt_f32_e32 vcc, v165, v153
	s_nop 0
	v_cndmask_b32_e64 v160, 0, 1, s[16:17]
	v_addc_co_u32_e32 v159, vcc, v159, v160, vcc
	v_cmp_gt_f32_e32 vcc, v166, v153
	s_nop 1
	v_cndmask_b32_e64 v160, 0, 1, vcc
	v_cmp_gt_f32_e32 vcc, v167, v153
	ds_read_b128 v[164:167], v154 offset:1904
	s_nop 0
	v_addc_co_u32_e32 v159, vcc, v159, v160, vcc
	s_waitcnt lgkmcnt(1)
	v_cmp_gt_f32_e64 s[16:17], v168, v153
	v_cmp_gt_f32_e32 vcc, v169, v153
	s_nop 0
	v_cndmask_b32_e64 v160, 0, 1, s[16:17]
	v_addc_co_u32_e32 v159, vcc, v159, v160, vcc
	v_cmp_gt_f32_e32 vcc, v170, v153
	s_nop 1
	v_cndmask_b32_e64 v160, 0, 1, vcc
	v_cmp_gt_f32_e32 vcc, v171, v153
	ds_read_b128 v[168:171], v154 offset:1920
	s_nop 0
	v_addc_co_u32_e32 v159, vcc, v159, v160, vcc
	s_waitcnt lgkmcnt(1)
	v_cmp_gt_f32_e64 s[16:17], v164, v153
	v_cmp_gt_f32_e32 vcc, v165, v153
	s_nop 0
	v_cndmask_b32_e64 v160, 0, 1, s[16:17]
	v_addc_co_u32_e32 v159, vcc, v159, v160, vcc
	v_cmp_gt_f32_e32 vcc, v166, v153
	s_nop 1
	v_cndmask_b32_e64 v160, 0, 1, vcc
	v_cmp_gt_f32_e32 vcc, v167, v153
	ds_read_b128 v[164:167], v154 offset:1936
	s_nop 0
	v_addc_co_u32_e32 v159, vcc, v159, v160, vcc
	s_waitcnt lgkmcnt(1)
	v_cmp_gt_f32_e64 s[16:17], v168, v153
	v_cmp_gt_f32_e32 vcc, v169, v153
	s_nop 0
	v_cndmask_b32_e64 v160, 0, 1, s[16:17]
	v_addc_co_u32_e32 v159, vcc, v159, v160, vcc
	v_cmp_gt_f32_e32 vcc, v170, v153
	s_nop 1
	v_cndmask_b32_e64 v160, 0, 1, vcc
	v_cmp_gt_f32_e32 vcc, v171, v153
	ds_read_b128 v[168:171], v154 offset:1952
	s_nop 0
	v_addc_co_u32_e32 v159, vcc, v159, v160, vcc
	s_waitcnt lgkmcnt(1)
	v_cmp_gt_f32_e64 s[16:17], v164, v153
	v_cmp_gt_f32_e32 vcc, v165, v153
	s_nop 0
	v_cndmask_b32_e64 v160, 0, 1, s[16:17]
	v_addc_co_u32_e32 v159, vcc, v159, v160, vcc
	v_cmp_gt_f32_e32 vcc, v166, v153
	s_nop 1
	v_cndmask_b32_e64 v160, 0, 1, vcc
	v_cmp_gt_f32_e32 vcc, v167, v153
	ds_read_b128 v[164:167], v154 offset:1968
	s_nop 0
	v_addc_co_u32_e32 v159, vcc, v159, v160, vcc
	s_waitcnt lgkmcnt(1)
	v_cmp_gt_f32_e64 s[16:17], v168, v153
	v_cmp_gt_f32_e32 vcc, v169, v153
	s_nop 0
	v_cndmask_b32_e64 v160, 0, 1, s[16:17]
	v_addc_co_u32_e32 v159, vcc, v159, v160, vcc
	v_cmp_gt_f32_e32 vcc, v170, v153
	s_nop 1
	v_cndmask_b32_e64 v160, 0, 1, vcc
	v_cmp_gt_f32_e32 vcc, v171, v153
	ds_read_b128 v[168:171], v154 offset:1984
	s_nop 0
	v_addc_co_u32_e32 v159, vcc, v159, v160, vcc
	s_waitcnt lgkmcnt(1)
	v_cmp_gt_f32_e32 vcc, v164, v153
	v_max_f32_e32 v160, v162, v162
	s_nop 0
	v_cndmask_b32_e64 v154, 0, 1, vcc
	v_cmp_gt_f32_e32 vcc, v165, v153
	s_nop 1
	v_addc_co_u32_e32 v154, vcc, v159, v154, vcc
	v_cmp_gt_f32_e64 s[16:17], v166, v153
	v_cmp_gt_f32_e32 vcc, v167, v153
	s_nop 0
	v_cndmask_b32_e64 v159, 0, 1, s[16:17]
	v_addc_co_u32_e32 v154, vcc, v154, v159, vcc
	s_waitcnt lgkmcnt(0)
	v_cmp_gt_f32_e64 s[16:17], v168, v153
	v_cmp_gt_f32_e32 vcc, v169, v153
	v_cmp_gt_f32_e64 s[98:99], v170, v153
	v_cndmask_b32_e64 v159, 0, 1, s[16:17]
	v_addc_co_u32_e32 v154, vcc, v154, v159, vcc
	v_cmp_gt_f32_e32 vcc, v171, v153
	v_cndmask_b32_e64 v159, 0, 1, s[98:99]
	s_nop 0
	v_addc_co_u32_e32 v154, vcc, v154, v159, vcc
	v_mov_b32_e32 v159, v201
	v_cmp_gt_u32_e32 vcc, 16, v154
	v_add_u32_e32 v154, 48, v154
	v_mov_b32_dpp v159, v162 row_ror:1 row_mask:0xf bank_mask:0xf
	v_max_f32_e32 v159, v159, v159
	v_max_f32_e32 v159, v160, v159
	v_mov_b32_e32 v160, v201
	s_and_b64 vcc, s[4:5], vcc
	v_cndmask_b32_e32 v154, v140, v154, vcc
	v_mov_b32_dpp v160, v159 row_ror:2 row_mask:0xf bank_mask:0xf
	v_max_f32_e32 v160, v160, v160
	v_max_f32_e32 v159, v159, v160
	v_mov_b32_e32 v160, v201
	v_lshlrev_b32_e32 v154, 2, v154
	ds_permute_b32 v153, v154, v153
	v_mov_b32_dpp v160, v159 row_ror:4 row_mask:0xf bank_mask:0xf
	v_max_f32_e32 v160, v160, v160
	v_max_f32_e32 v159, v159, v160
	v_mov_b32_e32 v160, v201
	ds_permute_b32 v154, v154, v156
	s_waitcnt lgkmcnt(1)
	v_cndmask_b32_e64 v153, v157, v153, s[50:51]
	v_mov_b32_dpp v160, v159 row_ror:8 row_mask:0xf bank_mask:0xf
	v_max_f32_e32 v160, v160, v160
	v_max_f32_e32 v159, v159, v160
	v_sub_f32_e32 v159, v162, v159
	v_mul_f32_e32 v159, 0x3fb8aa3b, v159
	v_exp_f32_e32 v159, v159
	s_waitcnt lgkmcnt(0)
	v_cndmask_b32_e64 v158, v155, v154, s[50:51]
	v_add_f32_dpp v156, v159, v159 row_ror:1 row_mask:0xf bank_mask:0xf bound_ctrl:1
	s_nop 1
	v_add_f32_dpp v156, v156, v156 row_ror:2 row_mask:0xf bank_mask:0xf bound_ctrl:1
	s_nop 1
	v_add_f32_dpp v156, v156, v156 row_ror:4 row_mask:0xf bank_mask:0xf bound_ctrl:1
	s_nop 1
	v_add_f32_dpp v156, v156, v156 row_ror:8 row_mask:0xf bank_mask:0xf bound_ctrl:1
	v_div_scale_f32 v160, s[80:81], v156, v156, v159
	v_rcp_f32_e32 v162, v160
	s_mov_b32 s80, 0x31200000
	v_fma_f32 v154, -v160, v162, 1.0
	v_fmac_f32_e32 v162, v154, v162
	v_div_scale_f32 v154, vcc, v159, v156, v159
	v_mul_f32_e32 v155, v154, v162
	v_fma_f32 v157, -v160, v155, v154
	v_fmac_f32_e32 v155, v157, v162
	v_fma_f32 v154, -v160, v155, v154
	v_mov_b32_e32 v157, v201
	v_div_fmas_f32 v154, v154, v162, v155
	v_div_fixup_f32 v156, v154, v156, v159
	v_mov_b32_dpp v157, v153 row_ror:1 row_mask:0xf bank_mask:0xf
	v_max_f32_e32 v159, v153, v153
	v_max_f32_e32 v157, v157, v157
	v_max_f32_e32 v157, v159, v157
	v_mov_b32_e32 v159, v201
	v_lshl_add_u64 v[154:155], s[92:93], 0, v[132:133]
	v_add_co_u32_e32 v154, vcc, s80, v154
	v_mov_b32_dpp v159, v157 row_ror:2 row_mask:0xf bank_mask:0xf
	v_max_f32_e32 v159, v159, v159
	v_max_f32_e32 v157, v157, v159
	v_mov_b32_e32 v159, v201
	v_addc_co_u32_e32 v155, vcc, 0, v155, vcc
	s_nop 0
	v_mov_b32_dpp v159, v157 row_ror:4 row_mask:0xf bank_mask:0xf
	v_max_f32_e32 v159, v159, v159
	v_max_f32_e32 v157, v157, v159
	v_mov_b32_e32 v159, v201
	global_store_dword v[154:155], v156, off
	s_nop 0
	v_mov_b32_dpp v159, v157 row_ror:8 row_mask:0xf bank_mask:0xf
	v_max_f32_e32 v159, v159, v159
	v_max_f32_e32 v157, v157, v159
	v_sub_f32_e32 v153, v153, v157
	v_mul_f32_e32 v153, 0x3fb8aa3b, v153
	v_exp_f32_e32 v153, v153
	s_nop 1
	v_add_f32_dpp v156, v153, v153 row_ror:1 row_mask:0xf bank_mask:0xf bound_ctrl:1
	s_nop 1
	v_add_f32_dpp v156, v156, v156 row_ror:2 row_mask:0xf bank_mask:0xf bound_ctrl:1
	s_nop 1
	v_add_f32_dpp v156, v156, v156 row_ror:4 row_mask:0xf bank_mask:0xf bound_ctrl:1
	s_nop 1
	v_add_f32_dpp v159, v156, v156 row_ror:8 row_mask:0xf bank_mask:0xf bound_ctrl:1
	v_div_scale_f32 v160, s[80:81], v159, v159, v153
	v_rcp_f32_e32 v162, v160
	v_lshl_add_u64 v[156:157], s[92:93], 0, v[134:135]
	global_store_dword v[156:157], v161, off
	v_fma_f32 v156, -v160, v162, 1.0
	v_fmac_f32_e32 v162, v156, v162
	v_div_scale_f32 v156, vcc, v153, v159, v153
	v_mul_f32_e32 v157, v156, v162
	v_fma_f32 v161, -v160, v157, v156
	v_fmac_f32_e32 v157, v161, v162
	v_fma_f32 v156, -v160, v157, v156
	v_div_fmas_f32 v156, v156, v162, v157
	v_div_fixup_f32 v153, v156, v159, v153
	global_store_dword v[154:155], v153, off offset:256
	v_lshlrev_b32_e32 v153, 7, v158
	v_lshl_add_u64 v[154:155], s[92:93], 0, v[136:137]
	s_and_b64 vcc, exec, s[52:53]
	global_store_dword v[154:155], v153, off
	s_cbranch_vccnz .LBB0_1847
	v_readlane_b32 s10, v254, 10
	v_readlane_b32 s11, v254, 11
	s_andn2_b64 vcc, exec, s[10:11]
	s_cbranch_vccnz .LBB0_1871
	global_load_dwordx4 v[164:167], v[112:113], off
	global_load_dwordx4 v[168:171], v[112:113], off offset:16
	global_load_dwordx4 v[172:175], v[112:113], off offset:32
	global_load_dwordx4 v[176:179], v[112:113], off offset:48
	global_load_dwordx4 v[180:183], v[114:115], off
	global_load_dwordx4 v[184:187], v[116:117], off
	global_load_dwordx4 v[188:191], v[118:119], off
	global_load_dwordx4 v[192:195], v[120:121], off
	s_waitcnt vmcnt(0)
	v_pk_mul_f32 v[46:47], v[46:47], v[166:167]
	v_pk_mul_f32 v[44:45], v[44:45], v[164:165]
	v_pk_mul_f32 v[42:43], v[42:43], v[170:171]
	v_pk_mul_f32 v[40:41], v[40:41], v[168:169]
	v_pk_mul_f32 v[38:39], v[38:39], v[174:175]
	v_pk_mul_f32 v[36:37], v[36:37], v[172:173]
	v_pk_mul_f32 v[34:35], v[34:35], v[178:179]
	v_pk_mul_f32 v[32:33], v[32:33], v[176:177]
	v_pk_mul_f32 v[50:51], v[50:51], v[182:183]
	v_pk_mul_f32 v[48:49], v[48:49], v[180:181]
	v_pk_mul_f32 v[62:63], v[62:63], v[186:187]
	v_pk_mul_f32 v[60:61], v[60:61], v[184:185]
	v_pk_mul_f32 v[58:59], v[58:59], v[190:191]
	v_pk_mul_f32 v[56:57], v[56:57], v[188:189]
	v_pk_mul_f32 v[54:55], v[54:55], v[194:195]
	v_pk_mul_f32 v[52:53], v[52:53], v[192:193]
